# k_bscatter/k_bfinal: wave prefix scans with DPP row_shr/row_bcast instead of 6 dependent ds_bpermute round trips
# speedup vs baseline: 1.0081x; 1.0081x over previous
.LBB0_90:
	s_or_b64 exec, exec, s[0:1]
	v_and_b32_e32 v7, 63, v0
	v_lshrrev_b32_e32 v14, 6, v0
	v_lshlrev_b32_e32 v20, 2, v14
	v_and_b32_e32 v4, 0x33f, v0
	v_cmp_eq_u32_e64 s[12:13], 63, v4
	v_mov_b32_e32 v3, v2
	s_nop 1
	v_add_u32_dpp v3, v3, v3 row_shr:1 row_mask:0xf bank_mask:0xf bound_ctrl:0
	s_nop 1
	v_add_u32_dpp v3, v3, v3 row_shr:2 row_mask:0xf bank_mask:0xf bound_ctrl:0
	s_nop 1
	v_add_u32_dpp v3, v3, v3 row_shr:4 row_mask:0xf bank_mask:0xf bound_ctrl:0
	s_nop 1
	v_add_u32_dpp v3, v3, v3 row_shr:8 row_mask:0xf bank_mask:0xf bound_ctrl:0
	s_nop 1
	v_add_u32_dpp v3, v3, v3 row_bcast:15 row_mask:0xa bank_mask:0xf
	s_nop 1
	v_add_u32_dpp v3, v3, v3 row_bcast:31 row_mask:0xc bank_mask:0xf
	s_and_saveexec_b64 s[14:15], s[12:13]
	ds_write_b32 v20, v3 offset:56496
	s_or_b64 exec, exec, s[14:15]
	s_waitcnt lgkmcnt(0)
	s_barrier
	s_and_saveexec_b64 s[28:29], vcc
	s_cbranch_execz .LBB0_100
	v_sub_u32_e32 v2, v3, v2
	v_cmp_lt_u32_e64 s[14:15], 63, v0
	s_and_saveexec_b64 s[30:31], s[14:15]
	s_cbranch_execz .LBB0_97
	s_mov_b32 s3, 0xdcb0
	s_mov_b64 s[34:35], 0
	v_mov_b32_e32 v3, v14

.LBB0_119:
	s_or_b64 exec, exec, s[2:3]
	s_waitcnt vmcnt(0)
	v_cmp_lt_i32_e64 s[20:21], -1, v22
	v_mov_b32_e32 v13, 0
	v_lshrrev_b32_e32 v29, 8, v22
	v_mov_b32_e32 v28, 0
	s_waitcnt lgkmcnt(0)
	s_barrier
	s_and_saveexec_b64 s[2:3], s[20:21]
	v_and_b32_e32 v8, 0xfffffc, v29
	v_mov_b32_e32 v12, 1
	ds_add_rtn_u32 v28, v8, v12 offset:55216
	s_or_b64 exec, exec, s[2:3]
	v_cmp_lt_i32_e64 s[18:19], -1, v23
	v_lshrrev_b32_e32 v8, 8, v23
	s_and_saveexec_b64 s[2:3], s[18:19]
	v_and_b32_e32 v12, 0xfffffc, v8
	v_mov_b32_e32 v13, 1
	ds_add_rtn_u32 v13, v12, v13 offset:55216
	s_or_b64 exec, exec, s[2:3]
	v_cmp_lt_i32_e64 s[16:17], -1, v24
	v_mov_b32_e32 v12, 0
	v_lshrrev_b32_e32 v27, 8, v24
	v_mov_b32_e32 v26, 0
	s_and_saveexec_b64 s[2:3], s[16:17]
	v_and_b32_e32 v25, 0xfffffc, v27
	v_mov_b32_e32 v26, 1
	ds_add_rtn_u32 v26, v25, v26 offset:55216
	s_or_b64 exec, exec, s[2:3]
	v_cmp_lt_i32_e64 s[14:15], -1, v10
	v_lshrrev_b32_e32 v25, 8, v10
	s_and_saveexec_b64 s[2:3], s[14:15]
	v_and_b32_e32 v12, 0xfffffc, v25
	v_mov_b32_e32 v30, 1
	ds_add_rtn_u32 v12, v12, v30 offset:55216
	s_or_b64 exec, exec, s[2:3]
	v_mov_b32_e32 v30, 0
	s_waitcnt lgkmcnt(0)
	s_barrier
	s_and_saveexec_b64 s[2:3], vcc
	ds_read_b32 v30, v6 offset:55216
	s_or_b64 exec, exec, s[2:3]
	s_waitcnt lgkmcnt(0)
	v_mov_b32_e32 v15, v30
	s_nop 1
	v_add_u32_dpp v15, v15, v15 row_shr:1 row_mask:0xf bank_mask:0xf bound_ctrl:0
	s_nop 1
	v_add_u32_dpp v15, v15, v15 row_shr:2 row_mask:0xf bank_mask:0xf bound_ctrl:0
	s_nop 1
	v_add_u32_dpp v15, v15, v15 row_shr:4 row_mask:0xf bank_mask:0xf bound_ctrl:0
	s_nop 1
	v_add_u32_dpp v15, v15, v15 row_shr:8 row_mask:0xf bank_mask:0xf bound_ctrl:0
	s_nop 1
	v_add_u32_dpp v15, v15, v15 row_bcast:15 row_mask:0xa bank_mask:0xf
	s_nop 1
	v_add_u32_dpp v15, v15, v15 row_bcast:31 row_mask:0xc bank_mask:0xf
	s_and_saveexec_b64 s[0:1], s[12:13]
	ds_write_b32 v20, v15 offset:56496
	s_or_b64 exec, exec, s[0:1]
	s_waitcnt lgkmcnt(0)
	s_barrier
	s_and_saveexec_b64 s[0:1], vcc
	s_cbranch_execz .LBB0_137
	v_sub_u32_e32 v15, v15, v30
	v_cmp_lt_u32_e32 vcc, 63, v0
	s_and_saveexec_b64 s[2:3], vcc
	s_cbranch_execz .LBB0_136
	s_mov_b32 s6, 0xdcb0
	s_mov_b64 s[4:5], 0

.LBB1_40:
	v_mbcnt_lo_u32_b32 v20, -1, 0
	s_load_dwordx4 s[20:23], s[0:1], 0x18
	s_load_dwordx2 s[28:29], s[0:1], 0x28
	s_waitcnt lgkmcnt(0)
	s_barrier
	ds_read_b32 v3, v1
	v_and_b32_e32 v33, 63, v0
	v_or_b32_e32 v21, 0x1000, v1
	v_lshrrev_b32_e32 v35, 6, v0
	v_lshlrev_b32_e32 v35, 2, v35
	v_cmp_gt_u32_e64 s[12:13], 16, v33
	s_waitcnt lgkmcnt(0)
	v_mov_b32_e32 v34, v3
	s_nop 1
	v_add_u32_dpp v34, v34, v34 row_shr:1 row_mask:0xf bank_mask:0xf bound_ctrl:0
	s_nop 1
	v_add_u32_dpp v34, v34, v34 row_shr:2 row_mask:0xf bank_mask:0xf bound_ctrl:0
	s_nop 1
	v_add_u32_dpp v34, v34, v34 row_shr:4 row_mask:0xf bank_mask:0xf bound_ctrl:0
	s_nop 1
	v_add_u32_dpp v34, v34, v34 row_shr:8 row_mask:0xf bank_mask:0xf bound_ctrl:0
	s_nop 1
	v_add_u32_dpp v34, v34, v34 row_bcast:15 row_mask:0xa bank_mask:0xf
	s_nop 1
	v_add_u32_dpp v34, v34, v34 row_bcast:31 row_mask:0xc bank_mask:0xf
	v_cmp_eq_u32_e64 s[14:15], 63, v33
	s_and_saveexec_b64 s[30:31], s[14:15]
	ds_write_b32 v35, v34 offset:12288
	s_or_b64 exec, exec, s[30:31]
	v_cmp_gt_u32_e64 s[14:15], 64, v0
	s_waitcnt lgkmcnt(0)
	s_barrier
	s_and_saveexec_b64 s[30:31], s[14:15]
	s_cbranch_execz .LBB1_47
	v_mov_b32_e32 v36, 0
	v_lshlrev_b32_e32 v33, 2, v33
	s_and_saveexec_b64 s[14:15], s[12:13]
	ds_read_b32 v36, v33 offset:12288
	s_or_b64 exec, exec, s[14:15]
	s_waitcnt lgkmcnt(0)
	v_mov_b32_e32 v20, v36
	s_nop 1
	v_add_u32_dpp v20, v20, v20 row_shr:1 row_mask:0xf bank_mask:0xf bound_ctrl:0
	s_nop 1
	v_add_u32_dpp v20, v20, v20 row_shr:2 row_mask:0xf bank_mask:0xf bound_ctrl:0
	s_nop 1
	v_add_u32_dpp v20, v20, v20 row_shr:4 row_mask:0xf bank_mask:0xf bound_ctrl:0
	s_nop 1
	v_add_u32_dpp v20, v20, v20 row_shr:8 row_mask:0xf bank_mask:0xf bound_ctrl:0
	s_and_b64 exec, exec, s[12:13]
	s_cbranch_execz .LBB1_47
	v_sub_u32_e32 v20, v20, v36
	ds_write_b32 v33, v20 offset:12288
